# mask
# baseline (speedup 1.0000x reference)
.LBB3_33:
	ds_read_b128 v[2:5], v217 offset:50176
	ds_read_b128 v[6:9], v217 offset:50304
	v_exp_f32_e32 v142, v142
	v_exp_f32_e32 v143, v143
	v_exp_f32_e32 v140, v140
	s_waitcnt vmcnt(1) lgkmcnt(1)
	v_mfma_f32_32x32x16_bf16 v[100:115], v[2:5], v[172:175], 0
	ds_read_b128 v[2:5], v217 offset:58880
	ds_read_b128 v[10:13], v217 offset:59008
	v_exp_f32_e32 v141, v141
	v_exp_f32_e32 v138, v138
	v_exp_f32_e32 v134, v134
	v_exp_f32_e32 v135, v135
	v_exp_f32_e32 v132, v132
	v_exp_f32_e32 v133, v133
	s_waitcnt lgkmcnt(1)
	v_mfma_f32_32x32x16_bf16 v[84:99], v[2:5], v[172:175], 0
	ds_read_b128 v[2:5], v217 offset:50208
	ds_read_b128 v[80:83], v217 offset:58912
	s_waitcnt vmcnt(0)
	ds_read_b128 v[116:119], v217 offset:50336
	v_exp_f32_e32 v130, v130
	v_exp_f32_e32 v131, v131
	v_exp_f32_e32 v128, v128
	v_exp_f32_e32 v129, v129
	s_sub_i32 s6, s60, 63
	s_waitcnt lgkmcnt(2)
	v_mfma_f32_32x32x16_bf16 v[100:115], v[2:5], v[168:171], v[100:115]
	ds_read_b128 v[2:5], v217 offset:59040
	ds_read_b128 v[120:123], v217 offset:50240
	ds_read_b128 v[124:127], v217 offset:50368
	ds_read_b128 v[230:233], v217 offset:58944
	ds_read_b128 v[234:237], v217 offset:59072
	ds_read_b128 v[238:241], v217 offset:50272
	ds_read_b128 v[242:245], v217 offset:50400
	s_waitcnt lgkmcnt(8)
	v_mfma_f32_32x32x16_bf16 v[84:99], v[80:83], v[168:171], v[84:99]
	ds_read_b128 v[80:83], v217 offset:58976
	ds_read_b128 v[246:249], v217 offset:59104
	s_waitcnt lgkmcnt(7)
	v_mfma_f32_32x32x16_bf16 v[100:115], v[120:123], v[164:167], v[100:115]
	v_add_f32_e32 v120, 0, v191
	v_add_f32_e32 v120, v193, v120
	v_add_f32_e32 v120, v189, v120
	v_add_f32_e32 v120, v192, v120
	v_add_f32_e32 v120, v188, v120
	v_add_f32_e32 v120, v190, v120
	v_add_f32_e32 v120, v186, v120
	s_waitcnt lgkmcnt(5)
	v_mfma_f32_32x32x16_bf16 v[84:99], v[230:233], v[164:167], v[84:99]
	v_add_f32_e32 v120, v187, v120
	v_add_f32_e32 v120, v179, v120
	v_add_f32_e32 v120, v184, v120
	v_exp_f32_e32 v122, v139
	v_exp_f32_e32 v123, v136
	v_exp_f32_e32 v136, v137
	s_waitcnt lgkmcnt(3)
	v_mfma_f32_32x32x16_bf16 v[100:115], v[238:241], v[148:151], v[100:115]
	s_waitcnt lgkmcnt(1)
	v_mfma_f32_32x32x16_bf16 v[84:99], v[80:83], v[148:151], v[84:99]
	v_add_f32_e32 v80, v177, v120
	v_add_f32_e32 v80, v182, v80
	v_add_f32_e32 v80, v176, v80
	v_add_f32_e32 v80, v185, v80
	v_add_f32_e32 v80, v178, v80
	v_add_f32_e32 v80, v183, v80
	v_add_f32_e32 v80, v142, v80
	v_mfma_f32_32x32x16_bf16 v[100:115], v[6:9], v[152:155], v[100:115]
	v_add_f32_e32 v6, v143, v80
	v_add_f32_e32 v6, v140, v6
	v_add_f32_e32 v6, v141, v6
	v_add_f32_e32 v6, v138, v6
	v_add_f32_e32 v6, v122, v6
	v_add_f32_e32 v6, v123, v6
	v_add_f32_e32 v6, v136, v6
	v_mfma_f32_32x32x16_bf16 v[84:99], v[10:13], v[152:155], v[84:99]
	v_add_f32_e32 v6, v134, v6
	v_add_f32_e32 v6, v135, v6
	v_add_f32_e32 v6, v132, v6
	v_add_f32_e32 v6, v133, v6
	v_add_f32_e32 v6, v130, v6
	v_add_f32_e32 v6, v131, v6
	v_add_f32_e32 v6, v128, v6
	v_mfma_f32_32x32x16_bf16 v[100:115], v[116:119], v[156:159], v[100:115]
	v_add_f32_e32 v199, v129, v6
	v_mov_b32_e32 v207, v199
	s_nop 1
	v_permlane32_swap_b32_e32 v199, v207
	v_cvt_pk_bf16_f32 v80, v191, v193
	v_cvt_pk_bf16_f32 v81, v189, v192
	v_cvt_pk_bf16_f32 v82, v188, v190
	v_mfma_f32_32x32x16_bf16 v[84:99], v[2:5], v[156:159], v[84:99]
	v_cvt_pk_bf16_f32 v83, v186, v187
	v_cvt_pk_bf16_f32 v116, v179, v184
	v_cvt_pk_bf16_f32 v117, v177, v182
	v_cvt_pk_bf16_f32 v118, v176, v185
	v_cvt_pk_bf16_f32 v119, v178, v183
	v_cvt_pk_bf16_f32 v120, v142, v143
	v_cvt_pk_bf16_f32 v121, v140, v141
	v_mfma_f32_32x32x16_bf16 v[100:115], v[124:127], v[160:163], v[100:115]
	v_cvt_pk_bf16_f32 v122, v138, v122
	v_cvt_pk_bf16_f32 v123, v123, v136
	v_cvt_pk_bf16_f32 v124, v134, v135
	v_cvt_pk_bf16_f32 v125, v132, v133
	v_cvt_pk_bf16_f32 v126, v130, v131
	v_cvt_pk_bf16_f32 v127, v128, v129
	v_permlane32_swap_b32_e32 v80, v82
	v_mfma_f32_32x32x16_bf16 v[84:99], v[234:237], v[160:163], v[84:99]
	v_permlane32_swap_b32_e32 v81, v83
	v_permlane32_swap_b32_e32 v116, v118
	v_permlane32_swap_b32_e32 v117, v119
	v_permlane32_swap_b32_e32 v120, v122
	v_mfma_f32_32x32x16_bf16 v[100:115], v[242:245], v[144:147], v[100:115]
	v_permlane32_swap_b32_e32 v121, v123
	v_permlane32_swap_b32_e32 v124, v126
	v_permlane32_swap_b32_e32 v125, v127
	s_waitcnt lgkmcnt(0)
	v_mfma_f32_32x32x16_bf16 v[84:99], v[246:249], v[144:147], v[84:99]
	v_add_u32_e32 v234, s60, v201
	v_add_u32_e32 v2, 1, v234
	v_add_u32_e32 v4, 33, v234
	v_ashrrev_i32_e32 v3, 31, v2
	v_ashrrev_i32_e32 v5, 31, v4
	v_lshlrev_b64 v[10:11], 8, v[2:3]
	v_lshlrev_b64 v[12:13], 8, v[4:5]
	v_lshl_add_u64 v[2:3], v[14:15], 0, v[10:11]
	v_lshl_add_u64 v[6:7], v[14:15], 0, v[12:13]
	v_lshl_add_u64 v[10:11], v[208:209], 0, v[10:11]
	global_load_dwordx4 v[2:5], v[2:3], off
	s_nop 0
	global_load_dwordx4 v[6:9], v[6:7], off
	v_lshl_add_u64 v[128:129], v[208:209], 0, v[12:13]
	global_load_dwordx4 v[10:13], v[10:11], off
	s_nop 0
	global_load_dwordx4 v[176:179], v[128:129], off
	ds_read_b64_tr_b16 v[128:129], v213 offset:0
	ds_read_b64_tr_b16 v[130:131], v213 offset:0x800
	ds_read_b64_tr_b16 v[132:133], v213 offset:0x1000
	ds_read_b64_tr_b16 v[134:135], v213 offset:0x1800
	ds_read_b64_tr_b16 v[136:137], v213 offset:0x2000
	ds_read_b64_tr_b16 v[138:139], v213 offset:0x2800
	ds_read_b64_tr_b16 v[140:141], v213 offset:0x3000
	ds_read_b64_tr_b16 v[142:143], v213 offset:0x3800
	s_nop 0
	s_waitcnt lgkmcnt(6)
	v_mfma_f32_32x32x16_bf16 v[64:79], v[80:83], v[128:131], v[64:79]
	ds_read_b64_tr_b16 v[128:129], v213 offset:0x200
	ds_read_b64_tr_b16 v[130:131], v213 offset:0xa00
	s_waitcnt lgkmcnt(6)
	v_mfma_f32_32x32x16_bf16 v[64:79], v[116:119], v[132:135], v[64:79]
	ds_read_b64_tr_b16 v[132:133], v213 offset:0x1200
	ds_read_b64_tr_b16 v[134:135], v213 offset:0x1a00
	s_waitcnt lgkmcnt(6)
	v_mfma_f32_32x32x16_bf16 v[64:79], v[120:123], v[136:139], v[64:79]
	ds_read_b64_tr_b16 v[136:137], v213 offset:0x2200
	ds_read_b64_tr_b16 v[138:139], v213 offset:0x2a00
	ds_read_b64_tr_b16 v[182:183], v213 offset:0x3200
	ds_read_b64_tr_b16 v[184:185], v213 offset:0x3a00
	s_waitcnt lgkmcnt(8)
	v_mfma_f32_32x32x16_bf16 v[64:79], v[124:127], v[140:143], v[64:79]
	s_waitcnt lgkmcnt(6)
	v_mfma_f32_32x32x16_bf16 v[48:63], v[80:83], v[128:131], v[48:63]
	ds_read_b64_tr_b16 v[128:129], v213 offset:0x400
	ds_read_b64_tr_b16 v[130:131], v213 offset:0xc00
	s_waitcnt lgkmcnt(6)
	v_mfma_f32_32x32x16_bf16 v[48:63], v[116:119], v[132:135], v[48:63]
	ds_read_b64_tr_b16 v[132:133], v213 offset:0x1400
	ds_read_b64_tr_b16 v[134:135], v213 offset:0x1c00
	s_waitcnt lgkmcnt(6)
	v_mfma_f32_32x32x16_bf16 v[48:63], v[120:123], v[136:139], v[48:63]
	ds_read_b64_tr_b16 v[136:137], v213 offset:0x2400
	ds_read_b64_tr_b16 v[138:139], v213 offset:0x2c00
	ds_read_b64_tr_b16 v[140:141], v213 offset:0x3400
	ds_read_b64_tr_b16 v[142:143], v213 offset:0x3c00
	s_waitcnt lgkmcnt(8)
	v_mfma_f32_32x32x16_bf16 v[48:63], v[124:127], v[182:185], v[48:63]
	s_waitcnt lgkmcnt(6)
	v_mfma_f32_32x32x16_bf16 v[32:47], v[80:83], v[128:131], v[32:47]
	ds_read_b64_tr_b16 v[128:129], v213 offset:0x600
	ds_read_b64_tr_b16 v[130:131], v213 offset:0xe00
	s_waitcnt lgkmcnt(6)
	v_mfma_f32_32x32x16_bf16 v[32:47], v[116:119], v[132:135], v[32:47]
	ds_read_b64_tr_b16 v[132:133], v213 offset:0x1600
	ds_read_b64_tr_b16 v[134:135], v213 offset:0x1e00
	s_waitcnt lgkmcnt(6)
	v_mfma_f32_32x32x16_bf16 v[32:47], v[120:123], v[136:139], v[32:47]
	ds_read_b64_tr_b16 v[136:137], v213 offset:0x2600
	ds_read_b64_tr_b16 v[138:139], v213 offset:0x2e00
	ds_read_b64_tr_b16 v[182:183], v213 offset:0x3600
	ds_read_b64_tr_b16 v[184:185], v213 offset:0x3e00
	s_waitcnt lgkmcnt(8)
	v_mfma_f32_32x32x16_bf16 v[32:47], v[124:127], v[140:143], v[32:47]
	s_waitcnt lgkmcnt(6)
	v_mfma_f32_32x32x16_bf16 v[16:31], v[80:83], v[128:131], v[16:31]
	s_cmp_le_i32 s60, s55
	s_cselect_b64 s[46:47], -1, 0
	s_cmp_gt_i32 s6, s56
	s_cselect_b64 s[6:7], -1, 0
	s_and_b64 s[6:7], s[46:47], s[6:7]
	s_and_b64 vcc, exec, s[6:7]
	s_waitcnt lgkmcnt(4)
	v_mfma_f32_32x32x16_bf16 v[16:31], v[116:119], v[132:135], v[16:31]
	s_waitcnt lgkmcnt(2)
	v_mfma_f32_32x32x16_bf16 v[16:31], v[120:123], v[136:139], v[16:31]
	s_waitcnt lgkmcnt(0)
	v_mfma_f32_32x32x16_bf16 v[16:31], v[124:127], v[182:185], v[16:31]
	s_cbranch_vccnz .LBB3_35
	v_add_u32_e32 v80, 123, v0
	v_cmp_ge_i32_e64 s[64:65], v80, 0
	v_cmp_ge_i32_e64 s[66:67], v80, 32
	v_cmp_ge_i32_e64 s[68:69], v80, 1
	v_cmp_ge_i32_e64 s[70:71], v80, 33
	v_cmp_ge_i32_e64 s[72:73], v80, 2
	v_cmp_ge_i32_e64 s[74:75], v80, 34
	v_cmp_ge_i32_e64 s[76:77], v80, 3
	v_cmp_ge_i32_e64 s[78:79], v80, 35
	v_cndmask_b32_e64 v100, v221, v100, s[64:65]
	v_cndmask_b32_e64 v84, v221, v84, s[66:67]
	v_cndmask_b32_e64 v101, v221, v101, s[68:69]
	v_cndmask_b32_e64 v85, v221, v85, s[70:71]
	v_cndmask_b32_e64 v102, v221, v102, s[72:73]
	v_cndmask_b32_e64 v86, v221, v86, s[74:75]
	v_cndmask_b32_e64 v103, v221, v103, s[76:77]
	v_cndmask_b32_e64 v87, v221, v87, s[78:79]
	v_cmp_ge_i32_e64 s[64:65], v80, 8
	v_cmp_ge_i32_e64 s[66:67], v80, 40
	v_cmp_ge_i32_e64 s[68:69], v80, 9
	v_cmp_ge_i32_e64 s[70:71], v80, 41
	v_cmp_ge_i32_e64 s[72:73], v80, 10
	v_cmp_ge_i32_e64 s[74:75], v80, 42
	v_cmp_ge_i32_e64 s[76:77], v80, 11
	v_cmp_ge_i32_e64 s[78:79], v80, 43
	v_cndmask_b32_e64 v104, v221, v104, s[64:65]
	v_cndmask_b32_e64 v88, v221, v88, s[66:67]
	v_cndmask_b32_e64 v105, v221, v105, s[68:69]
	v_cndmask_b32_e64 v89, v221, v89, s[70:71]
	v_cndmask_b32_e64 v106, v221, v106, s[72:73]
	v_cndmask_b32_e64 v90, v221, v90, s[74:75]
	v_cndmask_b32_e64 v107, v221, v107, s[76:77]
	v_cndmask_b32_e64 v91, v221, v91, s[78:79]
	v_cmp_ge_i32_e64 s[64:65], v80, 16
	v_cmp_ge_i32_e64 s[66:67], v80, 48
	v_cmp_ge_i32_e64 s[68:69], v80, 17
	v_cmp_ge_i32_e64 s[70:71], v80, 49
	v_cmp_ge_i32_e64 s[72:73], v80, 18
	v_cmp_ge_i32_e64 s[74:75], v80, 50
	v_cmp_ge_i32_e64 s[76:77], v80, 19
	v_cmp_ge_i32_e64 s[78:79], v80, 51
	v_cndmask_b32_e64 v108, v221, v108, s[64:65]
	v_cndmask_b32_e64 v92, v221, v92, s[66:67]
	v_cndmask_b32_e64 v109, v221, v109, s[68:69]
	v_cndmask_b32_e64 v93, v221, v93, s[70:71]
	v_cndmask_b32_e64 v110, v221, v110, s[72:73]
	v_cndmask_b32_e64 v94, v221, v94, s[74:75]
	v_cndmask_b32_e64 v111, v221, v111, s[76:77]
	v_cndmask_b32_e64 v95, v221, v95, s[78:79]
	v_cmp_ge_i32_e64 s[64:65], v80, 24
	v_cmp_ge_i32_e64 s[66:67], v80, 56
	v_cmp_ge_i32_e64 s[68:69], v80, 25
	v_cmp_ge_i32_e64 s[70:71], v80, 57
	v_cmp_ge_i32_e64 s[72:73], v80, 26
	v_cmp_ge_i32_e64 s[74:75], v80, 58
	v_cmp_ge_i32_e64 s[76:77], v80, 27
	v_cmp_ge_i32_e64 s[78:79], v80, 59
	v_cndmask_b32_e64 v112, v221, v112, s[64:65]
	v_cndmask_b32_e64 v96, v221, v96, s[66:67]
	v_cndmask_b32_e64 v113, v221, v113, s[68:69]
	v_cndmask_b32_e64 v97, v221, v97, s[70:71]
	v_cndmask_b32_e64 v114, v221, v114, s[72:73]
	v_cndmask_b32_e64 v98, v221, v98, s[74:75]
	v_cndmask_b32_e64 v115, v221, v115, s[76:77]
	v_cndmask_b32_e64 v99, v221, v99, s[78:79]

.LBB3_41:
	ds_read_b64_tr_b16 v[234:235], v213 offset:0x4000
	ds_read_b64_tr_b16 v[236:237], v213 offset:0x4800
	ds_read_b64_tr_b16 v[238:239], v213 offset:0x5000
	ds_read_b64_tr_b16 v[240:241], v213 offset:0x5800
	ds_read_b64_tr_b16 v[242:243], v213 offset:0x6000
	ds_read_b64_tr_b16 v[244:245], v213 offset:0x6800
	ds_read_b64_tr_b16 v[246:247], v213 offset:0x7000
	ds_read_b64_tr_b16 v[248:249], v213 offset:0x7800
	s_add_i32 s6, s60, 64
	s_add_i32 s61, s60, 1
	s_waitcnt lgkmcnt(6)
	v_mfma_f32_32x32x16_bf16 v[64:79], v[180:183], v[234:237], v[64:79]
	ds_read_b64_tr_b16 v[234:235], v213 offset:0x4200
	ds_read_b64_tr_b16 v[236:237], v213 offset:0x4a00
	s_waitcnt lgkmcnt(6)
	v_mfma_f32_32x32x16_bf16 v[64:79], v[184:187], v[238:241], v[64:79]
	ds_read_b64_tr_b16 v[238:239], v213 offset:0x5200
	ds_read_b64_tr_b16 v[240:241], v213 offset:0x5a00
	s_waitcnt lgkmcnt(6)
	v_mfma_f32_32x32x16_bf16 v[64:79], v[188:191], v[242:245], v[64:79]
	ds_read_b64_tr_b16 v[242:243], v213 offset:0x6200
	ds_read_b64_tr_b16 v[244:245], v213 offset:0x6a00
	ds_read_b64_tr_b16 v[250:251], v213 offset:0x7200
	ds_read_b64_tr_b16 v[252:253], v213 offset:0x7a00
	s_waitcnt lgkmcnt(8)
	v_mfma_f32_32x32x16_bf16 v[64:79], v[192:195], v[246:249], v[64:79]
	s_waitcnt lgkmcnt(6)
	v_mfma_f32_32x32x16_bf16 v[48:63], v[180:183], v[234:237], v[48:63]
	ds_read_b64_tr_b16 v[234:235], v213 offset:0x4400
	ds_read_b64_tr_b16 v[236:237], v213 offset:0x4c00
	s_waitcnt lgkmcnt(6)
	v_mfma_f32_32x32x16_bf16 v[48:63], v[184:187], v[238:241], v[48:63]
	ds_read_b64_tr_b16 v[238:239], v213 offset:0x5400
	ds_read_b64_tr_b16 v[240:241], v213 offset:0x5c00
	s_waitcnt lgkmcnt(6)
	v_mfma_f32_32x32x16_bf16 v[48:63], v[188:191], v[242:245], v[48:63]
	ds_read_b64_tr_b16 v[242:243], v213 offset:0x6400
	ds_read_b64_tr_b16 v[244:245], v213 offset:0x6c00
	ds_read_b64_tr_b16 v[246:247], v213 offset:0x7400
	ds_read_b64_tr_b16 v[248:249], v213 offset:0x7c00
	s_waitcnt lgkmcnt(8)
	v_mfma_f32_32x32x16_bf16 v[48:63], v[192:195], v[250:253], v[48:63]
	s_waitcnt lgkmcnt(6)
	v_mfma_f32_32x32x16_bf16 v[32:47], v[180:183], v[234:237], v[32:47]
	ds_read_b64_tr_b16 v[234:235], v213 offset:0x4600
	ds_read_b64_tr_b16 v[236:237], v213 offset:0x4e00
	s_waitcnt lgkmcnt(6)
	v_mfma_f32_32x32x16_bf16 v[32:47], v[184:187], v[238:241], v[32:47]
	ds_read_b64_tr_b16 v[238:239], v213 offset:0x5600
	ds_read_b64_tr_b16 v[240:241], v213 offset:0x5e00
	s_waitcnt lgkmcnt(6)
	v_mfma_f32_32x32x16_bf16 v[32:47], v[188:191], v[242:245], v[32:47]
	ds_read_b64_tr_b16 v[242:243], v213 offset:0x6600
	ds_read_b64_tr_b16 v[244:245], v213 offset:0x6e00
	ds_read_b64_tr_b16 v[250:251], v213 offset:0x7600
	ds_read_b64_tr_b16 v[252:253], v213 offset:0x7e00
	s_waitcnt lgkmcnt(8)
	v_mfma_f32_32x32x16_bf16 v[32:47], v[192:195], v[246:249], v[32:47]
	s_waitcnt lgkmcnt(6)
	v_mfma_f32_32x32x16_bf16 v[16:31], v[180:183], v[234:237], v[16:31]
	s_cmp_le_i32 s6, s55
	s_cselect_b64 s[6:7], -1, 0
	s_cmp_gt_i32 s61, s56
	s_cselect_b64 s[62:63], -1, 0
	s_and_b64 s[6:7], s[6:7], s[62:63]
	s_and_b64 vcc, exec, s[6:7]
	s_waitcnt lgkmcnt(4)
	v_mfma_f32_32x32x16_bf16 v[16:31], v[184:187], v[238:241], v[16:31]
	s_waitcnt lgkmcnt(2)
	v_mfma_f32_32x32x16_bf16 v[16:31], v[188:191], v[242:245], v[16:31]
	s_waitcnt lgkmcnt(0)
	v_mfma_f32_32x32x16_bf16 v[16:31], v[192:195], v[250:253], v[16:31]
	s_cbranch_vccnz .LBB3_43
	v_add_u32_e32 v180, 59, v0
	v_cmp_ge_i32_e64 s[64:65], v180, 0
	v_cmp_ge_i32_e64 s[66:67], v180, 32
	v_cmp_ge_i32_e64 s[68:69], v180, 1
	v_cmp_ge_i32_e64 s[70:71], v180, 33
	v_cmp_ge_i32_e64 s[72:73], v180, 2
	v_cmp_ge_i32_e64 s[74:75], v180, 34
	v_cmp_ge_i32_e64 s[76:77], v180, 3
	v_cmp_ge_i32_e64 s[78:79], v180, 35
	v_cndmask_b32_e64 v128, v221, v128, s[64:65]
	v_cndmask_b32_e64 v112, v221, v112, s[66:67]
	v_cndmask_b32_e64 v129, v221, v129, s[68:69]
	v_cndmask_b32_e64 v113, v221, v113, s[70:71]
	v_cndmask_b32_e64 v130, v221, v130, s[72:73]
	v_cndmask_b32_e64 v114, v221, v114, s[74:75]
	v_cndmask_b32_e64 v131, v221, v131, s[76:77]
	v_cndmask_b32_e64 v115, v221, v115, s[78:79]
	v_cmp_ge_i32_e64 s[64:65], v180, 8
	v_cmp_ge_i32_e64 s[66:67], v180, 40
	v_cmp_ge_i32_e64 s[68:69], v180, 9
	v_cmp_ge_i32_e64 s[70:71], v180, 41
	v_cmp_ge_i32_e64 s[72:73], v180, 10
	v_cmp_ge_i32_e64 s[74:75], v180, 42
	v_cmp_ge_i32_e64 s[76:77], v180, 11
	v_cmp_ge_i32_e64 s[78:79], v180, 43
	v_cndmask_b32_e64 v132, v221, v132, s[64:65]
	v_cndmask_b32_e64 v116, v221, v116, s[66:67]
	v_cndmask_b32_e64 v133, v221, v133, s[68:69]
	v_cndmask_b32_e64 v117, v221, v117, s[70:71]
	v_cndmask_b32_e64 v134, v221, v134, s[72:73]
	v_cndmask_b32_e64 v118, v221, v118, s[74:75]
	v_cndmask_b32_e64 v135, v221, v135, s[76:77]
	v_cndmask_b32_e64 v119, v221, v119, s[78:79]
	v_cmp_ge_i32_e64 s[64:65], v180, 16
	v_cmp_ge_i32_e64 s[66:67], v180, 48
	v_cmp_ge_i32_e64 s[68:69], v180, 17
	v_cmp_ge_i32_e64 s[70:71], v180, 49
	v_cmp_ge_i32_e64 s[72:73], v180, 18
	v_cmp_ge_i32_e64 s[74:75], v180, 50
	v_cmp_ge_i32_e64 s[76:77], v180, 19
	v_cmp_ge_i32_e64 s[78:79], v180, 51
	v_cndmask_b32_e64 v136, v221, v136, s[64:65]
	v_cndmask_b32_e64 v120, v221, v120, s[66:67]
	v_cndmask_b32_e64 v137, v221, v137, s[68:69]
	v_cndmask_b32_e64 v121, v221, v121, s[70:71]
	v_cndmask_b32_e64 v138, v221, v138, s[72:73]
	v_cndmask_b32_e64 v122, v221, v122, s[74:75]
	v_cndmask_b32_e64 v139, v221, v139, s[76:77]
	v_cndmask_b32_e64 v123, v221, v123, s[78:79]
	v_cmp_ge_i32_e64 s[64:65], v180, 24
	v_cmp_ge_i32_e64 s[66:67], v180, 56
	v_cmp_ge_i32_e64 s[68:69], v180, 25
	v_cmp_ge_i32_e64 s[70:71], v180, 57
	v_cmp_ge_i32_e64 s[72:73], v180, 26
	v_cmp_ge_i32_e64 s[74:75], v180, 58
	v_cmp_ge_i32_e64 s[76:77], v180, 27
	v_cmp_ge_i32_e64 s[78:79], v180, 59
	v_cndmask_b32_e64 v140, v221, v140, s[64:65]
	v_cndmask_b32_e64 v124, v221, v124, s[66:67]
	v_cndmask_b32_e64 v141, v221, v141, s[68:69]
	v_cndmask_b32_e64 v125, v221, v125, s[70:71]
	v_cndmask_b32_e64 v142, v221, v142, s[72:73]
	v_cndmask_b32_e64 v126, v221, v126, s[74:75]
	v_cndmask_b32_e64 v143, v221, v143, s[76:77]
	v_cndmask_b32_e64 v127, v221, v127, s[78:79]

	.amdhsa_kernel _ZN4attn10attn_splitI14__hip_bfloat16S1_EEvPKT_S4_S4_PT0_PfS7_PKjPjii
		.amdhsa_group_segment_fixed_size 2304
		.amdhsa_private_segment_fixed_size 0
		.amdhsa_kernarg_size 328
		.amdhsa_user_sgpr_count 2
		.amdhsa_user_sgpr_dispatch_ptr 0
		.amdhsa_user_sgpr_queue_ptr 0
		.amdhsa_user_sgpr_kernarg_segment_ptr 1
		.amdhsa_user_sgpr_dispatch_id 0
		.amdhsa_user_sgpr_kernarg_preload_length 0
		.amdhsa_user_sgpr_kernarg_preload_offset 0
		.amdhsa_user_sgpr_private_segment_size 0
		.amdhsa_uses_dynamic_stack 0
		.amdhsa_enable_private_segment 0
		.amdhsa_system_sgpr_workgroup_id_x 1
		.amdhsa_system_sgpr_workgroup_id_y 0
		.amdhsa_system_sgpr_workgroup_id_z 0
		.amdhsa_system_sgpr_workgroup_info 0
		.amdhsa_system_vgpr_workitem_id 2
		.amdhsa_next_free_vgpr 254
		.amdhsa_next_free_sgpr 80
		.amdhsa_accum_offset 256
		.amdhsa_reserve_vcc 1
		.amdhsa_float_round_mode_32 0
		.amdhsa_float_round_mode_16_64 0
		.amdhsa_float_denorm_mode_32 3
		.amdhsa_float_denorm_mode_16_64 3
		.amdhsa_dx10_clamp 1
		.amdhsa_ieee_mode 1
		.amdhsa_fp16_overflow 0
		.amdhsa_tg_split 0
		.amdhsa_exception_fp_ieee_invalid_op 0
		.amdhsa_exception_fp_denorm_src 0
		.amdhsa_exception_fp_ieee_div_zero 0
		.amdhsa_exception_fp_ieee_overflow 0
		.amdhsa_exception_fp_ieee_underflow 0
		.amdhsa_exception_fp_ieee_inexact 0
		.amdhsa_exception_int_div_zero 0
	.end_amdhsa_kernel

amdhsa.kernels:
  - .agpr_count:     0
    .args:
      - .offset:         0
        .size:           128
        .value_kind:     by_value
      - .actual_access:  read_only
        .address_space:  global
        .offset:         128
        .size:           8
        .value_kind:     global_buffer
      - .address_space:  global
        .offset:         136
        .size:           8
        .value_kind:     global_buffer
      - .offset:         144
        .size:           64
        .value_kind:     by_value
      - .offset:         208
        .size:           4
        .value_kind:     hidden_block_count_x
      - .offset:         212
        .size:           4
        .value_kind:     hidden_block_count_y
      - .offset:         216
        .size:           4
        .value_kind:     hidden_block_count_z
      - .offset:         220
        .size:           2
        .value_kind:     hidden_group_size_x
      - .offset:         222
        .size:           2
        .value_kind:     hidden_group_size_y
      - .offset:         224
        .size:           2
        .value_kind:     hidden_group_size_z
      - .offset:         226
        .size:           2
        .value_kind:     hidden_remainder_x
      - .offset:         228
        .size:           2
        .value_kind:     hidden_remainder_y
      - .offset:         230
        .size:           2
        .value_kind:     hidden_remainder_z
      - .offset:         248
        .size:           8
        .value_kind:     hidden_global_offset_x
      - .offset:         256
        .size:           8
        .value_kind:     hidden_global_offset_y
      - .offset:         264
        .size:           8
        .value_kind:     hidden_global_offset_z
      - .offset:         272
        .size:           2
        .value_kind:     hidden_grid_dims
    .group_segment_fixed_size: 16896
    .kernarg_segment_align: 8
    .kernarg_segment_size: 464
    .language:       OpenCL C
    .language_version:
      - 2
      - 0
    .max_flat_workgroup_size: 256
    .name:           _Z11prep_kernel7CvtArgsPKiPj6LnArgs
    .private_segment_fixed_size: 0
    .sgpr_count:     60
    .sgpr_spill_count: 0
    .symbol:         _Z11prep_kernel7CvtArgsPKiPj6LnArgs.kd
    .uniform_work_group_size: 1
    .uses_dynamic_stack: false
    .vgpr_count:     120
    .vgpr_spill_count: 0
    .wavefront_size: 64
  - .agpr_count:     0
    .args:
      - .actual_access:  read_only
        .address_space:  global
        .offset:         0
        .size:           8
        .value_kind:     global_buffer
      - .actual_access:  read_only
        .address_space:  global
        .offset:         8
        .size:           8
        .value_kind:     global_buffer
      - .actual_access:  write_only
        .address_space:  global
        .offset:         16
        .size:           8
        .value_kind:     global_buffer
      - .actual_access:  read_only
        .address_space:  global
        .offset:         24
        .size:           8
        .value_kind:     global_buffer
      - .offset:         32
        .size:           4
        .value_kind:     by_value
      - .actual_access:  read_only
        .address_space:  global
        .offset:         40
        .size:           8
        .value_kind:     global_buffer
      - .actual_access:  read_only
        .address_space:  global
        .offset:         48
        .size:           8
        .value_kind:     global_buffer
      - .actual_access:  read_only
        .address_space:  global
        .offset:         56
        .size:           8
        .value_kind:     global_buffer
      - .actual_access:  read_only
        .address_space:  global
        .offset:         64
        .size:           8
        .value_kind:     global_buffer
      - .offset:         72
        .size:           4
        .value_kind:     hidden_block_count_x
      - .offset:         76
        .size:           4
        .value_kind:     hidden_block_count_y
      - .offset:         80
        .size:           4
        .value_kind:     hidden_block_count_z
      - .offset:         84
        .size:           2
        .value_kind:     hidden_group_size_x
      - .offset:         86
        .size:           2
        .value_kind:     hidden_group_size_y
      - .offset:         88
        .size:           2
        .value_kind:     hidden_group_size_z
      - .offset:         90
        .size:           2
        .value_kind:     hidden_remainder_x
      - .offset:         92
        .size:           2
        .value_kind:     hidden_remainder_y
      - .offset:         94
        .size:           2
        .value_kind:     hidden_remainder_z
      - .offset:         112
        .size:           8
        .value_kind:     hidden_global_offset_x
      - .offset:         120
        .size:           8
        .value_kind:     hidden_global_offset_y
      - .offset:         128
        .size:           8
        .value_kind:     hidden_global_offset_z
      - .offset:         136
        .size:           2
        .value_kind:     hidden_grid_dims
    .group_segment_fixed_size: 32768
    .kernarg_segment_align: 8
    .kernarg_segment_size: 328
    .language:       OpenCL C
    .language_version:
      - 2
      - 0
    .max_flat_workgroup_size: 256
    .name:           _ZN4attn12attn_combineEPKfS1_PtPKjiPKtS6_S6_PKi
    .private_segment_fixed_size: 0
    .sgpr_count:     30
    .sgpr_spill_count: 0
    .symbol:         _ZN4attn12attn_combineEPKfS1_PtPKjiPKtS6_S6_PKi.kd
    .uniform_work_group_size: 1
    .uses_dynamic_stack: false
    .vgpr_count:     62
    .vgpr_spill_count: 0
    .wavefront_size: 64
  - .agpr_count:     0
    .args:
      - .actual_access:  read_only
        .address_space:  global
        .offset:         0
        .size:           8
        .value_kind:     global_buffer
      - .actual_access:  read_only
        .address_space:  global
        .offset:         8
        .size:           8
        .value_kind:     global_buffer
      - .offset:         16
        .size:           4
        .value_kind:     by_value
      - .offset:         20
        .size:           4
        .value_kind:     by_value
      - .offset:         24
        .size:           4
        .value_kind:     by_value
      - .offset:         32
        .size:           72
        .value_kind:     by_value
    .group_segment_fixed_size: 0
    .kernarg_segment_align: 8
    .kernarg_segment_size: 104
    .language:       OpenCL C
    .language_version:
      - 2
      - 0
    .max_flat_workgroup_size: 512
    .name:           _Z6gemm4pILi96ELi2ELi0EEvPKtS1_iii7EpiArgs
    .private_segment_fixed_size: 0
    .sgpr_count:     68
    .sgpr_spill_count: 0
    .symbol:         _Z6gemm4pILi96ELi2ELi0EEvPKtS1_iii7EpiArgs.kd
    .uniform_work_group_size: 1
    .uses_dynamic_stack: false
    .vgpr_count:     216
    .vgpr_spill_count: 0
    .wavefront_size: 64
  - .agpr_count:     0
    .args:
      - .actual_access:  read_only
        .address_space:  global
        .offset:         0
        .size:           8
        .value_kind:     global_buffer
      - .actual_access:  read_only
        .address_space:  global
        .offset:         8
        .size:           8
        .value_kind:     global_buffer
      - .actual_access:  read_only
        .address_space:  global
        .offset:         16
        .size:           8
        .value_kind:     global_buffer
      - .actual_access:  write_only
        .address_space:  global
        .offset:         24
        .size:           8
        .value_kind:     global_buffer
      - .actual_access:  write_only
        .address_space:  global
        .offset:         32
        .size:           8
        .value_kind:     global_buffer
      - .actual_access:  write_only
        .address_space:  global
        .offset:         40
        .size:           8
        .value_kind:     global_buffer
      - .actual_access:  read_only
        .address_space:  global
        .offset:         48
        .size:           8
        .value_kind:     global_buffer
      - .actual_access:  write_only
        .address_space:  global
        .offset:         56
        .size:           8
        .value_kind:     global_buffer
      - .offset:         64
        .size:           4
        .value_kind:     by_value
      - .offset:         68
        .size:           4
        .value_kind:     by_value
      - .offset:         72
        .size:           4
        .value_kind:     hidden_block_count_x
      - .offset:         76
        .size:           4
        .value_kind:     hidden_block_count_y
      - .offset:         80
        .size:           4
        .value_kind:     hidden_block_count_z
      - .offset:         84
        .size:           2
        .value_kind:     hidden_group_size_x
      - .offset:         86
        .size:           2
        .value_kind:     hidden_group_size_y
      - .offset:         88
        .size:           2
        .value_kind:     hidden_group_size_z
      - .offset:         90
        .size:           2
        .value_kind:     hidden_remainder_x
      - .offset:         92
        .size:           2
        .value_kind:     hidden_remainder_y
      - .offset:         94
        .size:           2
        .value_kind:     hidden_remainder_z
      - .offset:         112
        .size:           8
        .value_kind:     hidden_global_offset_x
      - .offset:         120
        .size:           8
        .value_kind:     hidden_global_offset_y
      - .offset:         128
        .size:           8
        .value_kind:     hidden_global_offset_z
      - .offset:         136
        .size:           2
        .value_kind:     hidden_grid_dims
      - .offset:         192
        .size:           4
        .value_kind:     hidden_dynamic_lds_size
    .group_segment_fixed_size: 2304
    .kernarg_segment_align: 8
    .kernarg_segment_size: 328
    .language:       OpenCL C
    .language_version:
      - 2
      - 0
    .max_flat_workgroup_size: 512
    .name:           _ZN4attn10attn_splitI14__hip_bfloat16S1_EEvPKT_S4_S4_PT0_PfS7_PKjPjii
    .private_segment_fixed_size: 0
    .sgpr_count:     86
    .sgpr_spill_count: 0
    .symbol:         _ZN4attn10attn_splitI14__hip_bfloat16S1_EEvPKT_S4_S4_PT0_PfS7_PKjPjii.kd
    .uniform_work_group_size: 1
    .uses_dynamic_stack: false
    .vgpr_count:     254
    .vgpr_spill_count: 0
    .wavefront_size: 64
  - .agpr_count:     0
    .args:
      - .actual_access:  read_only
        .address_space:  global
        .offset:         0
        .size:           8
        .value_kind:     global_buffer
      - .actual_access:  read_only
        .address_space:  global
        .offset:         8
        .size:           8
        .value_kind:     global_buffer
      - .offset:         16
        .size:           4
        .value_kind:     by_value
      - .offset:         20
        .size:           4
        .value_kind:     by_value
      - .offset:         24
        .size:           4
        .value_kind:     by_value
      - .offset:         32
        .size:           72
        .value_kind:     by_value
    .group_segment_fixed_size: 0
    .kernarg_segment_align: 8
    .kernarg_segment_size: 104
    .language:       OpenCL C
    .language_version:
      - 2
      - 0
    .max_flat_workgroup_size: 512
    .name:           _Z6gemm4pILi64ELi2ELi3EEvPKtS1_iii7EpiArgs
    .private_segment_fixed_size: 0
    .sgpr_count:     49
    .sgpr_spill_count: 0
    .symbol:         _Z6gemm4pILi64ELi2ELi3EEvPKtS1_iii7EpiArgs.kd
    .uniform_work_group_size: 1
    .uses_dynamic_stack: false
    .vgpr_count:     194
    .vgpr_spill_count: 0
    .wavefront_size: 64
  - .agpr_count:     0
    .args:
      - .actual_access:  read_only
        .address_space:  global
        .offset:         0
        .size:           8
        .value_kind:     global_buffer
      - .actual_access:  read_only
        .address_space:  global
        .offset:         8
        .size:           8
        .value_kind:     global_buffer
      - .offset:         16
        .size:           4
        .value_kind:     by_value
      - .offset:         20
        .size:           4
        .value_kind:     by_value
      - .offset:         24
        .size:           4
        .value_kind:     by_value
      - .offset:         32
        .size:           72
        .value_kind:     by_value
    .group_segment_fixed_size: 0
    .kernarg_segment_align: 8
    .kernarg_segment_size: 104
    .language:       OpenCL C
    .language_version:
      - 2
      - 0
    .max_flat_workgroup_size: 512
    .name:           _Z6gemm4pILi96ELi2ELi4EEvPKtS1_iii7EpiArgs
    .private_segment_fixed_size: 0
    .sgpr_count:     71
    .sgpr_spill_count: 0
    .symbol:         _Z6gemm4pILi96ELi2ELi4EEvPKtS1_iii7EpiArgs.kd
    .uniform_work_group_size: 1
    .uses_dynamic_stack: false
    .vgpr_count:     244
    .vgpr_spill_count: 0
    .wavefront_size: 64
  - .agpr_count:     0
    .args:
      - .actual_access:  read_only
        .address_space:  global
        .offset:         0
        .size:           8
        .value_kind:     global_buffer
      - .actual_access:  read_only
        .address_space:  global
        .offset:         8
        .size:           8
        .value_kind:     global_buffer
      - .offset:         16
        .size:           4
        .value_kind:     by_value
      - .offset:         20
        .size:           4
        .value_kind:     by_value
      - .offset:         24
        .size:           4
        .value_kind:     by_value
      - .offset:         32
        .size:           72
        .value_kind:     by_value
    .group_segment_fixed_size: 0
    .kernarg_segment_align: 8
    .kernarg_segment_size: 104
    .language:       OpenCL C
    .language_version:
      - 2
      - 0
    .max_flat_workgroup_size: 512
    .name:           _Z6gemm4pILi64ELi2ELi1EEvPKtS1_iii7EpiArgs
    .private_segment_fixed_size: 0
    .sgpr_count:     50
    .sgpr_spill_count: 0
    .symbol:         _Z6gemm4pILi64ELi2ELi1EEvPKtS1_iii7EpiArgs.kd
    .uniform_work_group_size: 1
    .uses_dynamic_stack: false
    .vgpr_count:     186
    .vgpr_spill_count: 0
    .wavefront_size: 64
